# warmkarg2
# baseline (speedup 1.0000x reference)
_Z11prep_kernelPKfS0_PKiS2_S0_S0_S0_S0_S0_S0_Pc:
	s_getpc_b64 s[36:37]
	s_add_u32 s36, s36, _Z11attn_kernelILi4EEvPKfS1_S1_S1_S1_S1_PKcPf@rel32@lo+4
	s_addc_u32 s37, s37, _Z11attn_kernelILi4EEvPKfS1_S1_S1_S1_S1_PKcPf@rel32@hi+12
	v_and_b32_e32 v192, 63, v0
	v_lshlrev_b32_e32 v192, 7, v192
	v_min_u32_e32 v192, 0x1180, v192
	global_load_dword v192, v192, s[36:37]
	s_lshr_b32 s4, s2, 2
	v_lshrrev_b32_e32 v2, 6, v0
	s_and_b32 s4, s4, 0x1ffffffe
	s_load_dwordx4 s[28:31], s[0:1], 0x40
	s_load_dwordx8 s[12:19], s[0:1], 0x0
	s_load_dwordx8 s[20:27], s[0:1], 0x20
	s_load_dwordx2 s[32:33], s[0:1], 0x50
	s_load_dword s40, s[0:1], 0x60
	s_load_dword s41, s[0:1], 0x9c
	v_and_b32_e32 v1, 15, v0
	s_and_b32 s3, s2, 7
	v_or_b32_e32 v2, s4, v2
	v_lshl_or_b32 v88, v2, 3, s3
	v_cmp_gt_u32_e64 s[10:11], 14, v1
	v_mul_lo_u32 v7, v88, 14
	v_and_b32_e32 v105, 63, v0
	v_cndmask_b32_e64 v6, 13, v1, s[10:11]
	v_add_u32_e32 v2, v7, v6
	v_mul_u32_u24_e32 v4, 12, v2
	v_lshlrev_b32_e32 v5, 2, v6
	v_cmp_gt_u32_e64 s[8:9], 48, v105
	v_cmp_gt_u32_e64 s[6:7], 14, v105
	v_lshlrev_b32_e32 v118, 1, v0
	v_lshrrev_b32_e32 v104, 4, v0
	v_cndmask_b32_e64 v8, 0, v105, s[8:9]
	v_cndmask_b32_e64 v9, 0, v105, s[6:7]
	v_mad_u32_u24 v8, v88, 48, v8
	v_add_lshl_u32 v9, v7, v9, 2
	v_lshlrev_b32_e32 v8, 2, v8
	s_lshl_b32 s2, s2, 3
	s_and_b32 s2, s2, 0x78
	v_and_b32_e32 v106, 30, v118
	v_or_b32_e32 v107, s2, v104
	v_cmp_gt_u32_e64 s[2:3], 23, v106
	v_or_b32_e32 v10, 1, v106
	v_cmp_gt_u32_e64 s[4:5], 23, v10
	v_lshlrev_b32_e32 v11, 7, v106
	v_lshlrev_b32_e32 v10, 7, v10
	v_cndmask_b32_e64 v11, 0, v11, s[2:3]
	v_cndmask_b32_e64 v10, 0, v10, s[4:5]
	v_or_b32_e32 v11, v11, v107
	v_or_b32_e32 v10, v10, v107
	v_lshlrev_b32_e32 v11, 2, v11
	v_lshlrev_b32_e32 v10, 2, v10
	v_lshlrev_b32_e32 v12, 2, v107
	v_lshlrev_b32_e32 v119, 5, v0
	v_lshlrev_b32_e32 v13, 2, v0
	v_and_b32_e32 v109, 12, v13
	v_and_b32_e32 v91, 0xf80, v119
	v_lshl_or_b32 v91, v109, 2, v91
	v_or_b32_e32 v92, 0x1000, v91
	v_lshlrev_b32_e32 v90, 9, v2
	v_and_b32_e32 v16, 48, v0
	v_or_b32_e32 v90, v90, v16
	v_or_b32_e32 v112, 0x80, v0
	v_or_b32_e32 v111, 0x180, v0
	v_or_b32_e32 v108, 0x280, v0
	v_mov_b32_e32 v87, 0
	v_bfe_u32 v110, v0, 4, 2
	s_movk_i32 s34, 0x60
	v_lshrrev_b32_e32 v136, 1, v0
	v_lshrrev_b32_e32 v18, 3, v0
	v_and_b32_e32 v18, 4, v18
	v_and_b32_e32 v19, 24, v0
	v_and_b32_e32 v20, 2, v136
	v_or3_b32 v18, v18, v19, v20
	v_and_or_b32 v136, v136, s34, v18
	v_mul_u32_u24_e32 v18, 0x110, v109
	v_lshl_add_u32 v136, v136, 1, v18
	v_add_u32_e32 v137, 0x1100, v136
	v_add_u32_e32 v138, 0x2200, v136
	v_lshlrev_b32_e32 v18, 9, v88
	v_and_b32_e32 v19, 0x100, v119
	v_lshlrev_b32_e32 v20, 4, v0
	v_and_b32_e32 v20, 48, v20
	v_or3_b32 v139, v18, v19, v20
	v_and_b32_e32 v19, 8, v118
	v_and_b32_e32 v20, 64, v118
	v_or3_b32 v139, v139, v19, v20
	v_lshlrev_b32_e32 v19, 2, v110
	v_and_b32_e32 v20, 4, v19
	v_or_b32_e32 v139, v139, v20
	v_lshl_or_b32 v140, v1, 5, v18
	v_or_b32_e32 v140, v140, v19
	v_add_u32_e32 v140, 0x80000, v140
	v_lshl_or_b32 v141, v88, 4, v1
	v_lshlrev_b32_e32 v141, 3, v141
	v_add_u32_e32 v141, 0x140000, v141
	v_lshlrev_b32_e32 v20, 8, v88
	v_mul_u32_u24_e32 v21, 43, v105
	v_lshrrev_b32_e32 v21, 9, v21
	v_mul_u32_u24_e32 v21, 12, v21
	v_sub_u32_e32 v22, v105, v21
	v_and_b32_e32 v142, 3, v22
	v_lshrrev_b32_e32 v22, 2, v22
	v_mad_u32_u24 v142, v142, 3, v22
	v_add_u32_e32 v142, v142, v21
	v_lshl_add_u32 v142, v142, 2, v20
	v_add_u32_e32 v142, 0x164000, v142
	v_lshl_add_u32 v143, v105, 2, v20
	v_add_u32_e32 v143, 0x164000, v143
	v_lshlrev_b32_e32 v123, 6, v107
	v_lshl_add_u32 v123, v106, 1, v123
	v_add_u32_e32 v123, 0x160000, v123
	v_lshl_add_u32 v122, v1, 4, v20
	v_or_b32_e32 v122, v122, v19
	v_add_u32_e32 v122, 0x100000, v122
	s_waitcnt lgkmcnt(0)
	global_load_dwordx3 v[82:84], v4, s[12:13]
	global_load_dword v85, v5, s[26:27]
	global_load_dword v114, v8, s[18:19]
	global_load_dword v115, v9, s[16:17]
	global_load_dword v116, v11, s[28:29]
	global_load_dword v113, v10, s[28:29]
	global_load_dword v117, v12, s[30:31]
	global_load_dwordx4 v[66:69], v91, s[20:21]
	global_load_dwordx4 v[70:73], v91, s[20:21] offset:64
	global_load_dwordx4 v[74:77], v92, s[20:21]
	global_load_dwordx4 v[78:81], v92, s[20:21] offset:64
	global_load_dwordx4 v[58:61], v91, s[22:23]
	global_load_dwordx4 v[62:65], v91, s[22:23] offset:64
	global_load_dwordx4 v[50:53], v92, s[22:23]
	global_load_dwordx4 v[54:57], v92, s[22:23] offset:64
	global_load_dwordx4 v[42:45], v91, s[24:25]
	global_load_dwordx4 v[46:49], v91, s[24:25] offset:64
	global_load_dwordx4 v[34:37], v92, s[24:25]
	global_load_dwordx4 v[38:41], v92, s[24:25] offset:64
	global_load_dwordx4 v[26:29], v90, s[14:15] nt
	global_load_dwordx4 v[30:33], v90, s[14:15] offset:64 nt
	global_load_dwordx4 v[18:21], v90, s[14:15] offset:128 nt
	global_load_dwordx4 v[22:25], v90, s[14:15] offset:192 nt
	global_load_dwordx4 v[10:13], v90, s[14:15] offset:256 nt
	global_load_dwordx4 v[14:17], v90, s[14:15] offset:320 nt
	global_load_dwordx4 v[2:5], v90, s[14:15] offset:384 nt
	global_load_dwordx4 v[6:9], v90, s[14:15] offset:448 nt
	s_waitcnt vmcnt(26)
	v_mov_b32_e32 v90, v83
	v_mov_b32_e32 v91, v84
	v_lshlrev_b32_e32 v86, 2, v110
	s_waitcnt vmcnt(25)
	v_mul_f32_e32 v84, 0x3fb8aa3b, v85
	s_mov_b32 s14, 0x41700000
	v_exp_f32_e32 v84, v84
	v_cndmask_b32_e64 v94, 0, 1.0, s[10:11]
	v_add_f32_e32 v84, 1.0, v84
	v_cmp_lt_f32_e32 vcc, s14, v85
	v_log_f32_e32 v84, v84
	v_cmp_lt_u32_e64 s[12:13], 15, v105
	v_mul_f32_e32 v84, 0x3f317218, v84
	v_cndmask_b32_e32 v84, v84, v85, vcc
	v_mul_f32_e32 v84, 0xbe715bef, v84
	v_mul_f32_e32 v84, 0x3f3504f3, v84
	v_mul_f32_e32 v84, 0x41800000, v84
	v_cndmask_b32_e64 v99, 0, v84, s[10:11]
	v_mul_f32_e32 v101, -2.0, v99
	v_mul_f32_e32 v100, v82, v82
	v_cmp_gt_u32_e32 vcc, 16, v105
	v_fmac_f32_e32 v100, v90, v90
	v_cmp_eq_u32_e64 s[12:13], 0, v110
	v_fmac_f32_e32 v100, v91, v91
	v_cmp_eq_u32_e64 s[14:15], 1, v110
	v_mul_f32_e32 v83, v101, v82
	v_cmp_eq_u32_e64 s[16:17], 2, v110
	v_mul_f32_e32 v84, v101, v90
	v_mul_f32_e32 v85, v101, v91
	v_mul_f32_e32 v89, v99, v100
	v_mul_f32_e32 v92, v82, v94
	v_mul_f32_e32 v93, v90, v94
	v_mul_f32_e32 v95, v91, v94
	v_mul_f32_e32 v96, v100, v94
	v_cvt_pk_fp8_f32 v88, v83, v83
	v_cvt_pk_fp8_f32 v104, v84, v84
	v_cvt_f32_fp8_e32 v97, v88
	v_cvt_f32_fp8_e32 v98, v104
	v_sub_f32_e32 v97, v83, v97
	v_sub_f32_e32 v98, v84, v98
	v_cvt_pk_fp8_f32 v88, v85, v85
	v_cvt_pk_fp8_f32 v104, v99, v99
	v_cvt_f32_fp8_e32 v101, v88
	v_cvt_f32_fp8_e32 v102, v104
	v_sub_f32_e32 v101, v85, v101
	v_sub_f32_e32 v102, v99, v102
	v_cvt_pk_fp8_f32 v88, v89, v89
	v_cvt_pk_fp8_f32 v104, v92, v92
	v_cvt_f32_fp8_e32 v103, v88
	v_cvt_f32_fp8_e32 v120, v104
	v_sub_f32_e32 v103, v89, v103
	v_sub_f32_e32 v120, v92, v120
	v_cvt_pk_fp8_f32 v88, v93, v93
	v_cvt_pk_fp8_f32 v104, v95, v95
	v_cvt_f32_fp8_e32 v121, v88
	v_cvt_f32_fp8_e32 v86, v104
	v_sub_f32_e32 v121, v93, v121
	v_sub_f32_e32 v86, v95, v86
	v_cvt_pk_fp8_f32 v88, v96, v96
	s_nop 0
	v_cvt_f32_fp8_e32 v87, v88
	s_nop 0
	v_sub_f32_e32 v87, v96, v87
	v_cndmask_b32_e64 v124, v89, v85, s[16:17]
	v_cndmask_b32_e64 v124, v124, v98, s[14:15]
	v_cndmask_b32_e64 v124, v124, v83, s[12:13]
	v_cndmask_b32_e64 v125, v103, v99, s[16:17]
	v_cndmask_b32_e64 v125, v125, v84, s[14:15]
	v_cndmask_b32_e64 v125, v125, v97, s[12:13]
	v_cndmask_b32_e64 v126, 0, v102, s[16:17]
	v_cndmask_b32_e64 v126, v126, v85, s[14:15]
	v_cndmask_b32_e64 v126, v126, v83, s[12:13]
	v_cndmask_b32_e64 v127, 0, v99, s[16:17]
	v_cndmask_b32_e64 v127, v127, v101, s[14:15]
	v_cndmask_b32_e64 v127, v127, v84, s[12:13]
	v_cndmask_b32_e64 v128, v94, v86, s[16:17]
	v_cndmask_b32_e64 v128, v128, v93, s[14:15]
	v_cndmask_b32_e64 v128, v128, v92, s[12:13]
	v_cndmask_b32_e64 v129, v94, v96, s[16:17]
	v_cndmask_b32_e64 v129, v129, v121, s[14:15]
	v_cndmask_b32_e64 v129, v129, v92, s[12:13]
	v_cndmask_b32_e64 v130, 0, v96, s[16:17]
	v_cndmask_b32_e64 v130, v130, v95, s[14:15]
	v_cndmask_b32_e64 v130, v130, v120, s[12:13]
	v_cndmask_b32_e64 v131, 0, v87, s[16:17]
	v_cndmask_b32_e64 v131, v131, v95, s[14:15]
	v_cndmask_b32_e64 v131, v131, v93, s[12:13]
	v_cvt_pk_fp8_f32 v119, v124, v125
	v_cvt_pk_fp8_f32 v103, v128, v129
	v_cvt_pk_fp8_f32 v119, v126, v127 op_sel:[0,0,1]
	v_cvt_pk_fp8_f32 v103, v130, v131 op_sel:[0,0,1]
	s_nop 0
	global_store_dword v139, v119, s[32:33] offset:128
	global_store_dword v140, v103, s[32:33] offset:16
	s_and_saveexec_b64 s[0:1], vcc
	s_cbranch_execz .LBB0_14
	v_cvt_f16_f32_e32 v83, v82
	v_cvt_pk_f16_f32 v90, v90, v91
	s_nop 0
	v_alignbit_b32 v91, 0, v90, 16
	v_pack_b32_f16 v90, v83, v90
	global_store_dwordx2 v141, v[90:91], s[32:33]
